# layer-0 prep RMSNorm of x: norm-gain vector loaded once before the row loop instead of four serialized loads (each behind a vmcnt(0)) per row
# baseline (speedup 1.0000x reference)
; __device__ __forceinline__ unsigned cvt_pk_bf16(float lo, float hi) { unsigned r; asm volatile("v_cvt_pk_bf16_f32 %0, %1, %2" : "=v"(r) : "v"(lo), "v"(hi)); return r; }
; __device__ __forceinline__ void norm_row_nx(const float* hrow, float* hcopy, const float* g, bf16* NX, int t, int lane) {
;     const f32x4* xr = (const f32x4*)hrow + lane; f32x4 v[4]; float s = 0.f;
; #pragma unroll
;     for (int j = 0; j < 4; ++j) { v[j] = xr[64 * j]; s += (v[j].x * v[j].x + v[j].y * v[j].y) + (v[j].z * v[j].z + v[j].w * v[j].w); }
;     if (hcopy) {
; #pragma unroll
;         for (int j = 0; j < 4; ++j) ((f32x4*)hcopy)[lane + 64 * j] = v[j]; }
;     const float rstd = 1.f / sqrtf(wave_sum(s) * (1.f / D) + 1e-6f);
; #pragma unroll
;     for (int j = 0; j < 4; ++j) { const f32x4 gv = ((const f32x4*)g)[lane + 64 * j]; const f32x4 o = v[j] * rstd * gv;
;         v2u w; w.x = cvt_pk_bf16(o.x, o.y); w.y = cvt_pk_bf16(o.z, o.w);
;         const int c = 4 * (lane + 64 * j);
;         *(v2u*)(NX + NXROW(t) * 1024 + c) = w; }
; }
; __device__ __forceinline__ void prep_phase(Frame& F, const Args& a, int layer, int blk, int nblk_, int part) {
;     ...
;     if (layer == 0 && (part & 1)) {
;         if (gw < NB) *(v4u*)((bf16*)(ws + WS_NX) + (size_t)gw * (SEQ + 1) * 1024 + 8 * lane) = (v4u){0u, 0u, 0u, 0u}, *(v4u*)((bf16*)(ws + WS_NX) + (size_t)gw * (SEQ + 1) * 1024 + 512 + 8 * lane) = (v4u){0u, 0u, 0u, 0u};
;         for (int m = gw; m < T; m += NGW) norm_row_nx(a.in[0] + (size_t)m * D, F.h + (size_t)m * D, a.in[2], (bf16*)(ws + WS_NX), m, lane);
;     }
.LBB0_109:
	s_cmpk_gt_i32 s60, 0x7fff
	s_cbranch_scc1 .LBB0_114
	s_cmp_lg_u64 s[24:25], 0
	v_ashrrev_i32_e32 v1, 31, v0
	v_readlane_b32 s36, v251, 2
	s_cselect_b64 s[0:1], -1, 0
	v_lshlrev_b64 v[0:1], 4, v[0:1]
	v_readlane_b32 s40, v251, 6
	v_readlane_b32 s41, v251, 7
	s_lshl_b64 s[4:5], s[60:61], 12
	v_add_u32_e32 v18, 0x100, v16
	v_add_u32_e32 v20, 0x200, v16
	v_add_u32_e32 v22, 0x300, v16
	v_lshl_add_u64 v[24:25], s[40:41], 0, v[0:1]
	s_ashr_i32 s83, s82, 31
	v_lshl_add_u64 v[26:27], s[4:5], 0, v[0:1]
	v_cndmask_b32_e64 v0, 0, 1, s[0:1]
	v_ashrrev_i32_e32 v17, 31, v16
	v_ashrrev_i32_e32 v19, 31, v18
	v_ashrrev_i32_e32 v21, 31, v20
	v_ashrrev_i32_e32 v23, 31, v22
	s_lshl_b64 s[6:7], s[82:83], 12
	v_cmp_ne_u32_e64 s[0:1], 1, v0
	v_mov_b32_e32 v28, 0x358637bd
	s_mov_b32 s12, 0xf800000
	v_mov_b32_e32 v29, 0x260
	s_mov_b64 s[8:9], s[60:61]
	v_readlane_b32 s37, v251, 3
	v_readlane_b32 s38, v251, 4
	v_readlane_b32 s39, v251, 5
	v_readlane_b32 s42, v251, 8
	v_readlane_b32 s43, v251, 9
	v_readlane_b32 s44, v251, 10
	v_readlane_b32 s45, v251, 11
	v_readlane_b32 s46, v251, 12
	v_readlane_b32 s47, v251, 13
	v_readlane_b32 s48, v251, 14
	v_readlane_b32 s49, v251, 15
	v_readlane_b32 s50, v251, 16
	v_readlane_b32 s51, v251, 17
	global_load_dwordx4 v[132:135], v[24:25], off
	global_load_dwordx4 v[136:139], v[24:25], off offset:1024
	global_load_dwordx4 v[140:143], v[24:25], off offset:2048
	global_load_dwordx4 v[144:147], v[24:25], off offset:3072
	s_waitcnt vmcnt(0)
	s_branch .LBB0_112
.LBB0_111:
	s_waitcnt vmcnt(3)
	v_mul_f32_e32 v34, v13, v13
	v_mul_f32_e32 v35, v15, v15
	s_waitcnt vmcnt(2)
	v_mul_f32_e32 v36, v9, v9
	v_mul_f32_e32 v37, v11, v11
	s_waitcnt vmcnt(1)
	v_mul_f32_e32 v38, v5, v5
	v_mul_f32_e32 v39, v7, v7
	v_fmac_f32_e32 v34, v12, v12
	v_fmac_f32_e32 v35, v14, v14
	v_fmac_f32_e32 v36, v8, v8
	v_fmac_f32_e32 v37, v10, v10
	s_waitcnt vmcnt(0)
	v_mul_f32_e32 v40, v1, v1
	v_mul_f32_e32 v41, v3, v3
	v_fmac_f32_e32 v38, v4, v4
	v_fmac_f32_e32 v39, v6, v6
	v_add_f32_e32 v34, v34, v35
	v_add_f32_e32 v35, v36, v37
	v_fmac_f32_e32 v40, v0, v0
	v_fmac_f32_e32 v41, v2, v2
	v_add_f32_e32 v36, v38, v39
	v_add_f32_e32 v34, v34, v35
	v_add_f32_e32 v37, v40, v41
	v_add_f32_e32 v34, v34, v36
	v_add_f32_e32 v34, v34, v37
	s_lshr_b64 s[4:5], s[8:9], 12
	s_add_u32 s4, s8, s4
	v_add_f32_dpp v34, v34, v34 quad_perm:[1,0,3,2] row_mask:0xf bank_mask:0xf bound_ctrl:1
	s_addc_u32 s5, s9, s5
	s_lshl_b64 s[4:5], s[4:5], 11
	v_add_f32_dpp v34, v34, v34 quad_perm:[2,3,0,1] row_mask:0xf bank_mask:0xf bound_ctrl:1
	s_add_u32 s4, s18, s4
	s_addc_u32 s5, s19, s5
	v_add_f32_dpp v34, v34, v34 row_half_mirror row_mask:0xf bank_mask:0xf bound_ctrl:1
	s_add_u32 s10, s4, 0x12400800
	s_addc_u32 s11, s5, 0
	v_add_f32_dpp v34, v34, v34 row_mirror row_mask:0xf bank_mask:0xf bound_ctrl:1
	v_mov_b32_e32 v35, v34
	s_nop 1
	v_permlane16_swap_b32_e32 v34, v35
	v_add_f32_e32 v34, v34, v35
	v_mov_b32_e32 v35, v34
	s_nop 1
	v_permlane32_swap_b32_e32 v34, v35
	v_add_f32_e32 v34, v34, v35
	v_fmamk_f32 v34, v34, 0x3a800000, v28
	v_mul_f32_e32 v35, 0x4f800000, v34
	v_cmp_gt_f32_e32 vcc, s12, v34
	s_add_u32 s8, s8, s82
	s_addc_u32 s9, s9, s83
	v_cndmask_b32_e32 v34, v34, v35, vcc
	v_sqrt_f32_e32 v35, v34
	s_cmp_lt_i32 s8, 0x8000
	v_lshl_add_u64 v[26:27], v[26:27], 0, s[6:7]
	v_add_u32_e32 v36, -1, v35
	v_add_u32_e32 v37, 1, v35
	v_fma_f32 v38, -v36, v35, v34
	v_fma_f32 v39, -v37, v35, v34
	v_cmp_ge_f32_e64 s[4:5], 0, v38
	s_nop 1
	v_cndmask_b32_e64 v35, v35, v36, s[4:5]
	v_cmp_lt_f32_e64 s[4:5], 0, v39
	s_nop 1
	v_cndmask_b32_e64 v35, v35, v37, s[4:5]
	v_mul_f32_e32 v36, 0x37800000, v35
	v_cndmask_b32_e32 v35, v35, v36, vcc
	v_cmp_class_f32_e32 vcc, v34, v29
	s_nop 1
	v_cndmask_b32_e32 v36, v35, v34, vcc
	v_div_scale_f32 v37, s[4:5], v36, v36, 1.0
	v_rcp_f32_e32 v38, v37
	v_div_scale_f32 v39, vcc, 1.0, v36, 1.0
	v_lshl_add_u64 v[34:35], v[16:17], 1, s[10:11]
	v_fma_f32 v40, -v37, v38, 1.0
	v_fmac_f32_e32 v38, v40, v38
	v_mul_f32_e32 v40, v39, v38
	v_fma_f32 v41, -v37, v40, v39
	v_fmac_f32_e32 v40, v41, v38
	v_fma_f32 v37, -v37, v40, v39
	v_div_fmas_f32 v37, v37, v38, v40
	v_div_fixup_f32 v36, v37, v36, 1.0
	v_pk_mul_f32 v[12:13], v[12:13], v[36:37] op_sel_hi:[1,0]
	v_pk_mul_f32 v[14:15], v[14:15], v[36:37] op_sel_hi:[1,0]
	v_pk_mul_f32 v[12:13], v[132:133], v[12:13]
	v_pk_mul_f32 v[14:15], v[134:135], v[14:15]
	v_cvt_pk_bf16_f32 v12, v12, v13
	v_pk_mul_f32 v[8:9], v[8:9], v[36:37] op_sel_hi:[1,0]
	v_cvt_pk_bf16_f32 v13, v14, v15
	global_store_dwordx2 v[34:35], v[12:13], off
	v_lshl_add_u64 v[30:31], v[18:19], 1, s[10:11]
	v_pk_mul_f32 v[10:11], v[10:11], v[36:37] op_sel_hi:[1,0]
	v_pk_mul_f32 v[4:5], v[4:5], v[36:37] op_sel_hi:[1,0]
	v_pk_mul_f32 v[6:7], v[6:7], v[36:37] op_sel_hi:[1,0]
	v_pk_mul_f32 v[0:1], v[0:1], v[36:37] op_sel_hi:[1,0]
	v_pk_mul_f32 v[2:3], v[2:3], v[36:37] op_sel_hi:[1,0]
	v_pk_mul_f32 v[8:9], v[136:137], v[8:9]
	v_pk_mul_f32 v[10:11], v[138:139], v[10:11]
	v_cvt_pk_bf16_f32 v8, v8, v9
	v_lshl_add_u64 v[12:13], v[20:21], 1, s[10:11]
	v_cvt_pk_bf16_f32 v9, v10, v11
	global_store_dwordx2 v[30:31], v[8:9], off
	v_pk_mul_f32 v[4:5], v[140:141], v[4:5]
	v_pk_mul_f32 v[6:7], v[142:143], v[6:7]
	v_cvt_pk_bf16_f32 v4, v4, v5
	v_lshl_add_u64 v[8:9], v[22:23], 1, s[10:11]
	v_cvt_pk_bf16_f32 v5, v6, v7
	global_store_dwordx2 v[12:13], v[4:5], off
	v_pk_mul_f32 v[0:1], v[0:1], v[144:145]
	v_pk_mul_f32 v[2:3], v[2:3], v[146:147]
	v_cvt_pk_bf16_f32 v0, v0, v1
	s_nop 0
	v_cvt_pk_bf16_f32 v1, v2, v3
	global_store_dwordx2 v[8:9], v[0:1], off
	s_cbranch_scc0 .LBB0_114
